# P14 K-loop: saddr LDS-DMA and stage loads rebalanced 4+4 per super-phase (A halves in SP1, B halves in SP2); plus P8 ladder and P7 hoist
# speedup vs baseline: 1.0117x; 1.0117x over previous
.LBB0_1671:
	s_cmp_lt_i32 s94, 15
	s_cselect_b64 s[0:1], -1, 0
	s_and_b64 s[0:1], s[0:1], s[4:5]
	s_andn2_b64 vcc, exec, s[0:1]
	s_cbranch_vccnz .LBB0_1688
	v_mov_b32_e32 v11, v0
	s_cmpk_gt_i32 s2, 0x157f
	v_mov_b32_e32 v1, 0x7f7f7f7f
	v_readfirstlane_b32 s5, v11
	s_cbranch_scc1 .LBB0_1688
	v_lshlrev_b32_e32 v2, 4, v11
	v_add_u32_e32 v3, 0x2000, v2
	v_ashrrev_i32_e32 v4, 31, v3
	v_lshrrev_b32_e32 v4, 22, v4
	v_add_u32_e32 v4, v3, v4
	v_ashrrev_i32_e32 v10, 10, v4
	v_mul_i32_i24_e32 v4, 0x400, v10
	v_sub_u32_e32 v3, v3, v4
	v_lshrrev_b32_e32 v4, 4, v3
	v_bitop3_b32 v3, v4, v3, 32 bitop3:0x6c
	v_ashrrev_i32_e32 v4, 31, v3
	v_lshrrev_b32_e32 v4, 26, v4
	v_add_u32_e32 v4, v3, v4
	v_lshlrev_b32_e32 v5, 3, v10
	v_ashrrev_i32_e32 v12, 6, v4
	v_and_b32_e32 v5, -16, v5
	v_add_u32_e32 v5, v12, v5
	v_and_b32_e32 v6, 3, v12
	s_mov_b32 s4, 0xfffe0
	v_lshrrev_b32_e32 v7, 2, v5
	v_lshlrev_b32_e32 v8, 1, v5
	v_and_b32_e32 v4, 0xc0, v4
	v_and_or_b32 v6, v5, s4, v6
	v_and_b32_e32 v7, 4, v7
	v_and_b32_e32 v8, 24, v8
	v_sub_u32_e32 v3, v3, v4
	v_mov_b32_e32 v4, 1
	v_or3_b32 v6, v6, v7, v8
	v_lshlrev_b32_e32 v7, 5, v10
	v_ashrrev_i16_sdwa v3, v4, sext(v3) dst_sel:DWORD dst_unused:UNUSED_PAD src0_sel:DWORD src1_sel:BYTE_0
	v_and_b32_e32 v7, 32, v7
	v_bfe_i32 v13, v3, 0, 16
	v_add_lshl_u32 v3, v7, v13, 1
	v_lshl_add_u32 v162, v6, 12, v3
	v_lshl_add_u32 v164, v5, 12, v3
	v_bfe_i32 v3, v11, 27, 1
	v_lshrrev_b32_e32 v3, 22, v3
	v_add_u32_e32 v3, v2, v3
	v_and_b32_e32 v3, 0xfffffc00, v3
	v_sub_u32_e32 v2, v2, v3
	v_lshrrev_b32_e32 v3, 4, v2
	v_ashrrev_i32_e32 v5, 31, v11
	v_bitop3_b32 v2, v3, v2, 32 bitop3:0x6c
	v_lshrrev_b32_e32 v5, 26, v5
	v_ashrrev_i32_e32 v3, 31, v2
	v_add_u32_e32 v5, v11, v5
	v_lshrrev_b32_e32 v3, 26, v3
	v_ashrrev_i32_e32 v15, 6, v5
	v_add_u32_e32 v3, v2, v3
	v_lshlrev_b32_e32 v5, 3, v15
	v_ashrrev_i32_e32 v14, 6, v3
	v_and_b32_e32 v5, -16, v5
	v_add_u32_e32 v5, v14, v5
	v_and_b32_e32 v6, 3, v14
	s_ashr_i32 s15, s2, 31
	v_and_or_b32 v6, v5, s4, v6
	s_lshr_b32 s4, s15, 29
	s_add_i32 s4, s2, s4
	s_ashr_i32 s8, s5, 6
	s_ashr_i32 s6, s4, 3
	s_and_b32 s4, s4, -8
	s_ashr_i32 s12, s5, 8
	s_lshl_b32 s3, s8, 10
	s_sub_i32 s4, s2, s4
	s_cmp_lt_i32 s4, 0
	s_movk_i32 s17, 0x2b1
	s_cselect_b32 s7, s17, 0x2b0
	s_mul_i32 s4, s4, s7
	s_add_i32 s4, s4, s6
	s_mul_hi_i32 s6, s4, 0x2fa0be83
	s_lshr_b32 s7, s6, 31
	s_ashr_i32 s6, s6, 7
	s_add_i32 s6, s6, s7
	s_lshl_b32 s7, s6, 3
	s_mulk_i32 s6, 0x2b0
	s_sub_i32 s6, s4, s6
	s_sext_i32_i16 s4, s6
	s_bfe_u32 s4, s4, 0x3001c
	s_add_i32 s9, s6, s4
	s_sext_i32_i16 s4, s9
	s_and_b32 s9, s9, 0xfff8
	s_sub_i32 s6, s6, s9
	s_sext_i32_i16 s6, s6
	v_lshrrev_b32_e32 v7, 2, v5
	v_lshlrev_b32_e32 v8, 1, v5
	v_and_b32_e32 v3, 0xc0, v3
	s_lshr_b32 s4, s4, 3
	s_add_i32 s28, s7, s6
	v_and_b32_e32 v7, 4, v7
	v_and_b32_e32 v8, 24, v8
	v_sub_u32_e32 v2, v2, v3
	s_ashr_i32 s29, s28, 31
	s_bfe_i64 s[18:19], s[4:5], 0x100000
	v_or3_b32 v6, v6, v7, v8
	v_lshlrev_b32_e32 v7, 5, v15
	v_ashrrev_i16_sdwa v2, v4, sext(v2) dst_sel:DWORD dst_unused:UNUSED_PAD src0_sel:DWORD src1_sel:BYTE_0
	s_lshl_b64 s[6:7], s[28:29], 20
	s_lshl_b64 s[18:19], s[18:19], 20
	v_and_b32_e32 v7, 32, v7
	v_bfe_i32 v16, v2, 0, 16
	s_add_u32 s34, s88, s18
	v_add_lshl_u32 v2, v7, v16, 1
	s_addc_u32 s35, s89, s19
	s_add_i32 s29, s3, 0
	v_lshl_add_u32 v166, v6, 12, v2
	s_add_i32 m0, s29, 0x10000
	v_lshl_add_u32 v168, v5, 12, v2
	global_load_lds_dwordx4 v166, s[34:35]
	s_add_i32 m0, s29, 0x12000
	s_add_u32 s18, s34, 0x80000
	global_load_lds_dwordx4 v162, s[34:35]
	s_addc_u32 s19, s35, 0
	s_add_i32 m0, s29, 0x14000
	v_mov_b32_e32 v167, 0
	global_load_lds_dwordx4 v166, s[18:19]
	s_add_i32 m0, s29, 0x16000
	s_add_u32 s30, s54, s6
	s_addc_u32 s31, s55, s7
	s_add_i32 s38, s29, 0x2000
	global_load_lds_dwordx4 v162, s[18:19]
	s_mov_b32 m0, s29
	s_add_u32 s6, s30, 0x80000
	global_load_lds_dwordx4 v168, s[30:31]
	s_mov_b32 m0, s38
	s_addc_u32 s7, s31, 0
	s_add_i32 s39, s29, 0x4000
	global_load_lds_dwordx4 v164, s[30:31]
	s_mov_b32 m0, s39
	s_add_i32 s40, s29, 0x6000
	global_load_lds_dwordx4 v168, s[6:7]
	s_mov_b32 m0, s40
	v_mov_b32_e32 v163, v167
	global_load_lds_dwordx4 v164, s[6:7]
	v_mov_b32_e32 v169, v167
	v_mov_b32_e32 v165, v167
	s_add_u32 s100, s30, 0x80
	s_addc_u32 s101, s31, 0
	s_cmp_eq_u32 s12, 1
	s_mov_b32 s41, 0
	v_lshl_add_u64 v[8:9], s[34:35], 0, v[166:167]
	v_lshl_add_u64 v[6:7], s[34:35], 0, v[162:163]
	v_lshl_add_u64 v[2:3], s[30:31], 0, v[168:169]
	s_cselect_b64 s[6:7], -1, 0
	s_cmp_lg_u32 s12, 1
	v_lshl_add_u64 v[4:5], s[30:31], 0, v[164:165]
	s_cbranch_scc1 .LBB0_1675
	s_barrier

.LBB0_1681:
	ds_read_b128 v[26:29], v189
	ds_read_b128 v[30:33], v189 offset:1024
	ds_read_b128 v[18:21], v189 offset:2048
	ds_read_b128 v[22:25], v189 offset:3072
	ds_read_b128 v[10:13], v190
	ds_read_b128 v[14:17], v190 offset:1024
	ds_read_b128 v[2:5], v190 offset:2048
	ds_read_b128 v[6:9], v190 offset:3072
	s_add_u32 s34, s30, 0xfff80080
	s_addc_u32 s35, s31, -1
	s_cmp_eq_u32 s60, 28
	s_cselect_b32 s37, s18, s35
	s_cselect_b32 s36, s19, s34
	s_cselect_b32 s35, s21, s59
	s_cselect_b32 s34, s23, s58
	s_mov_b32 m0, s43
	s_nop 0
	global_load_lds_dwordx4 v168, s[100:101]
	s_mov_b32 m0, s44
	s_nop 0
	global_load_lds_dwordx4 v164, s[100:101]
	s_add_i32 m0, s29, 0xc000
	ds_read_b128 v[178:181], v191
	ds_read_b128 v[182:185], v191 offset:1024
	ds_read_b128 v[194:197], v191 offset:2048
	ds_read_b128 v[198:201], v191 offset:3072
	ds_read_b128 v[202:205], v191 offset:4096
	ds_read_b128 v[206:209], v191 offset:5120
	ds_read_b128 v[210:213], v191 offset:6144
	ds_read_b128 v[214:217], v191 offset:7168
	global_load_lds_dwordx4 v170, s[30:31]
	s_add_i32 m0, s29, 0xe000
	s_nop 0
	global_load_lds_dwordx4 v172, s[30:31]
	s_waitcnt vmcnt(8)
	s_waitcnt lgkmcnt(0)
	s_barrier
	s_setprio 1
	s_waitcnt lgkmcnt(0)
	v_mfma_scale_f32_16x16x128_f8f6f4 v[158:161], v[26:33], v[178:185], v[158:161], v1, v1 op_sel_hi:[0,0,0]
	v_mfma_scale_f32_16x16x128_f8f6f4 v[154:157], v[18:25], v[178:185], v[154:157], v1, v1 op_sel_hi:[0,0,0]
	v_mfma_scale_f32_16x16x128_f8f6f4 v[142:145], v[26:33], v[194:201], v[142:145], v1, v1 op_sel_hi:[0,0,0]
	v_mfma_scale_f32_16x16x128_f8f6f4 v[138:141], v[18:25], v[194:201], v[138:141], v1, v1 op_sel_hi:[0,0,0]
	v_mfma_scale_f32_16x16x128_f8f6f4 v[126:129], v[26:33], v[202:209], v[126:129], v1, v1 op_sel_hi:[0,0,0]
	v_mfma_scale_f32_16x16x128_f8f6f4 v[122:125], v[18:25], v[202:209], v[122:125], v1, v1 op_sel_hi:[0,0,0]
	v_mfma_scale_f32_16x16x128_f8f6f4 v[110:113], v[26:33], v[210:217], v[110:113], v1, v1 op_sel_hi:[0,0,0]
	v_mfma_scale_f32_16x16x128_f8f6f4 v[106:109], v[18:25], v[210:217], v[106:109], v1, v1 op_sel_hi:[0,0,0]
	s_setprio 0
	s_setprio 1
	v_mfma_scale_f32_16x16x128_f8f6f4 v[150:153], v[10:17], v[178:185], v[150:153], v1, v1 op_sel_hi:[0,0,0]
	v_mfma_scale_f32_16x16x128_f8f6f4 v[146:149], v[2:9], v[178:185], v[146:149], v1, v1 op_sel_hi:[0,0,0]
	v_mfma_scale_f32_16x16x128_f8f6f4 v[134:137], v[10:17], v[194:201], v[134:137], v1, v1 op_sel_hi:[0,0,0]
	v_mfma_scale_f32_16x16x128_f8f6f4 v[130:133], v[2:9], v[194:201], v[130:133], v1, v1 op_sel_hi:[0,0,0]
	v_mfma_scale_f32_16x16x128_f8f6f4 v[118:121], v[10:17], v[202:209], v[118:121], v1, v1 op_sel_hi:[0,0,0]
	v_mfma_scale_f32_16x16x128_f8f6f4 v[114:117], v[2:9], v[202:209], v[114:117], v1, v1 op_sel_hi:[0,0,0]
	v_mfma_scale_f32_16x16x128_f8f6f4 v[102:105], v[10:17], v[210:217], v[102:105], v1, v1 op_sel_hi:[0,0,0]
	v_mfma_scale_f32_16x16x128_f8f6f4 v[98:101], v[2:9], v[210:217], v[98:101], v1, v1 op_sel_hi:[0,0,0]
	s_setprio 0
	s_barrier
	s_add_i32 s61, s45, s3
	s_mov_b32 m0, s61
	ds_read_b128 v[194:197], v191 offset:16384
	ds_read_b128 v[198:201], v191 offset:17408
	ds_read_b128 v[202:205], v191 offset:18432
	ds_read_b128 v[206:209], v191 offset:19456
	ds_read_b128 v[210:213], v191 offset:20480
	ds_read_b128 v[214:217], v191 offset:21504
	ds_read_b128 v[218:221], v191 offset:22528
	ds_read_b128 v[222:225], v191 offset:23552
	global_load_lds_dwordx4 v166, s[34:35]
	s_add_i32 m0, s61, 0x2000
	s_add_u32 s62, s34, 0x80000
	s_addc_u32 s63, s35, 0
	s_add_i32 s61, s48, s3
	global_load_lds_dwordx4 v162, s[34:35]
	s_mov_b32 m0, s61
	s_nop 0
	global_load_lds_dwordx4 v166, s[62:63]
	s_add_i32 m0, s61, 0x2000
	s_nop 0
	global_load_lds_dwordx4 v162, s[62:63]
	s_waitcnt vmcnt(6)
	s_waitcnt lgkmcnt(0)
	s_barrier
	s_setprio 1
	s_waitcnt lgkmcnt(0)
	v_mfma_scale_f32_16x16x128_f8f6f4 v[94:97], v[26:33], v[194:201], v[94:97], v1, v1 op_sel_hi:[0,0,0]
	v_mfma_scale_f32_16x16x128_f8f6f4 v[90:93], v[18:25], v[194:201], v[90:93], v1, v1 op_sel_hi:[0,0,0]
	v_mfma_scale_f32_16x16x128_f8f6f4 v[78:81], v[26:33], v[202:209], v[78:81], v1, v1 op_sel_hi:[0,0,0]
	v_mfma_scale_f32_16x16x128_f8f6f4 v[74:77], v[18:25], v[202:209], v[74:77], v1, v1 op_sel_hi:[0,0,0]
	v_mfma_scale_f32_16x16x128_f8f6f4 v[62:65], v[26:33], v[210:217], v[62:65], v1, v1 op_sel_hi:[0,0,0]
	v_mfma_scale_f32_16x16x128_f8f6f4 v[58:61], v[18:25], v[210:217], v[58:61], v1, v1 op_sel_hi:[0,0,0]
	v_mfma_scale_f32_16x16x128_f8f6f4 v[46:49], v[26:33], v[218:225], v[46:49], v1, v1 op_sel_hi:[0,0,0]
	v_mfma_scale_f32_16x16x128_f8f6f4 v[42:45], v[18:25], v[218:225], v[42:45], v1, v1 op_sel_hi:[0,0,0]
	s_setprio 0
	s_setprio 1
	v_mfma_scale_f32_16x16x128_f8f6f4 v[86:89], v[10:17], v[194:201], v[86:89], v1, v1 op_sel_hi:[0,0,0]
	v_mfma_scale_f32_16x16x128_f8f6f4 v[82:85], v[2:9], v[194:201], v[82:85], v1, v1 op_sel_hi:[0,0,0]
	v_mfma_scale_f32_16x16x128_f8f6f4 v[70:73], v[10:17], v[202:209], v[70:73], v1, v1 op_sel_hi:[0,0,0]
	v_mfma_scale_f32_16x16x128_f8f6f4 v[66:69], v[2:9], v[202:209], v[66:69], v1, v1 op_sel_hi:[0,0,0]
	v_mfma_scale_f32_16x16x128_f8f6f4 v[54:57], v[10:17], v[210:217], v[54:57], v1, v1 op_sel_hi:[0,0,0]
	v_mfma_scale_f32_16x16x128_f8f6f4 v[50:53], v[2:9], v[210:217], v[50:53], v1, v1 op_sel_hi:[0,0,0]
	v_mfma_scale_f32_16x16x128_f8f6f4 v[38:41], v[10:17], v[218:225], v[38:41], v1, v1 op_sel_hi:[0,0,0]
	v_mfma_scale_f32_16x16x128_f8f6f4 v[34:37], v[2:9], v[218:225], v[34:37], v1, v1 op_sel_hi:[0,0,0]
	s_setprio 0
	s_barrier
	s_add_i32 s61, 0, 0x18000
	s_add_i32 s62, 0, 0x1c000
	v_add_u32_e32 v14, s61, v187
	v_add_u32_e32 v30, s62, v187
	ds_read_b128 v[2:5], v14
	ds_read_b128 v[6:9], v14 offset:1024
	ds_read_b128 v[10:13], v14 offset:2048
	ds_read_b128 v[14:17], v14 offset:3072
	ds_read_b128 v[18:21], v30
	ds_read_b128 v[22:25], v30 offset:1024
	ds_read_b128 v[26:29], v30 offset:2048
	ds_read_b128 v[30:33], v30 offset:3072
	s_mov_b32 m0, s29
	s_nop 0
	global_load_lds_dwordx4 v168, s[36:37]
	s_mov_b32 m0, s38
	s_nop 0
	global_load_lds_dwordx4 v164, s[36:37]
	s_add_u32 s36, s36, 0x80000
	s_addc_u32 s37, s37, 0
	s_add_u32 s100, s36, 0xfff80080
	s_addc_u32 s101, s37, -1
	s_mov_b32 m0, s39
	ds_read_b128 v[194:197], v191 offset:32768
	ds_read_b128 v[198:201], v191 offset:33792
	ds_read_b128 v[202:205], v191 offset:34816
	ds_read_b128 v[206:209], v191 offset:35840
	ds_read_b128 v[210:213], v191 offset:36864
	ds_read_b128 v[214:217], v191 offset:37888
	ds_read_b128 v[218:221], v191 offset:38912
	ds_read_b128 v[222:225], v191 offset:39936
	global_load_lds_dwordx4 v168, s[36:37]
	s_mov_b32 m0, s40
	s_nop 0
	global_load_lds_dwordx4 v164, s[36:37]
	s_waitcnt vmcnt(8)
	s_waitcnt lgkmcnt(0)
	s_barrier
	s_setprio 1
	s_waitcnt lgkmcnt(0)
	v_mfma_scale_f32_16x16x128_f8f6f4 v[158:161], v[2:9], v[194:201], v[158:161], v1, v1 op_sel_hi:[0,0,0]
	v_mfma_scale_f32_16x16x128_f8f6f4 v[154:157], v[10:17], v[194:201], v[154:157], v1, v1 op_sel_hi:[0,0,0]
	v_mfma_scale_f32_16x16x128_f8f6f4 v[142:145], v[2:9], v[202:209], v[142:145], v1, v1 op_sel_hi:[0,0,0]
	v_mfma_scale_f32_16x16x128_f8f6f4 v[138:141], v[10:17], v[202:209], v[138:141], v1, v1 op_sel_hi:[0,0,0]
	v_mfma_scale_f32_16x16x128_f8f6f4 v[126:129], v[2:9], v[210:217], v[126:129], v1, v1 op_sel_hi:[0,0,0]
	v_mfma_scale_f32_16x16x128_f8f6f4 v[122:125], v[10:17], v[210:217], v[122:125], v1, v1 op_sel_hi:[0,0,0]
	v_mfma_scale_f32_16x16x128_f8f6f4 v[110:113], v[2:9], v[218:225], v[110:113], v1, v1 op_sel_hi:[0,0,0]
	v_mfma_scale_f32_16x16x128_f8f6f4 v[106:109], v[10:17], v[218:225], v[106:109], v1, v1 op_sel_hi:[0,0,0]
	s_setprio 0
	s_setprio 1
	v_mfma_scale_f32_16x16x128_f8f6f4 v[150:153], v[18:25], v[194:201], v[150:153], v1, v1 op_sel_hi:[0,0,0]
	v_mfma_scale_f32_16x16x128_f8f6f4 v[146:149], v[26:33], v[194:201], v[146:149], v1, v1 op_sel_hi:[0,0,0]
	v_mfma_scale_f32_16x16x128_f8f6f4 v[134:137], v[18:25], v[202:209], v[134:137], v1, v1 op_sel_hi:[0,0,0]
	v_mfma_scale_f32_16x16x128_f8f6f4 v[130:133], v[26:33], v[202:209], v[130:133], v1, v1 op_sel_hi:[0,0,0]
	v_mfma_scale_f32_16x16x128_f8f6f4 v[118:121], v[18:25], v[210:217], v[118:121], v1, v1 op_sel_hi:[0,0,0]
	v_mfma_scale_f32_16x16x128_f8f6f4 v[114:117], v[26:33], v[210:217], v[114:117], v1, v1 op_sel_hi:[0,0,0]
	v_mfma_scale_f32_16x16x128_f8f6f4 v[102:105], v[18:25], v[218:225], v[102:105], v1, v1 op_sel_hi:[0,0,0]
	v_mfma_scale_f32_16x16x128_f8f6f4 v[98:101], v[26:33], v[218:225], v[98:101], v1, v1 op_sel_hi:[0,0,0]
	s_setprio 0
	s_barrier
	s_add_i32 s36, s61, s3
	s_mov_b32 m0, s36
	s_add_u32 s98, s34, 0x80
	s_addc_u32 s99, s35, 0
	ds_read_b128 v[194:197], v191 offset:49152
	ds_read_b128 v[198:201], v191 offset:50176
	ds_read_b128 v[202:205], v191 offset:51200
	ds_read_b128 v[206:209], v191 offset:52224
	ds_read_b128 v[210:213], v191 offset:53248
	ds_read_b128 v[214:217], v191 offset:54272
	ds_read_b128 v[218:221], v191 offset:55296
	ds_read_b128 v[222:225], v191 offset:56320
	global_load_lds_dwordx4 v166, s[98:99]
	s_add_i32 m0, s36, 0x2000
	s_add_u32 s34, s34, 0x80080
	s_addc_u32 s35, s35, 0
	s_add_i32 s36, s62, s3
	global_load_lds_dwordx4 v162, s[98:99]
	s_mov_b32 m0, s36
	s_nop 0
	global_load_lds_dwordx4 v166, s[34:35]
	s_add_i32 m0, s36, 0x2000
	s_nop 0
	global_load_lds_dwordx4 v162, s[34:35]
	s_waitcnt vmcnt(6)
	s_waitcnt lgkmcnt(0)
	s_barrier
	s_setprio 1
	s_waitcnt lgkmcnt(0)
	v_mfma_scale_f32_16x16x128_f8f6f4 v[94:97], v[2:9], v[194:201], v[94:97], v1, v1 op_sel_hi:[0,0,0]
	v_mfma_scale_f32_16x16x128_f8f6f4 v[90:93], v[10:17], v[194:201], v[90:93], v1, v1 op_sel_hi:[0,0,0]
	v_mfma_scale_f32_16x16x128_f8f6f4 v[78:81], v[2:9], v[202:209], v[78:81], v1, v1 op_sel_hi:[0,0,0]
	v_mfma_scale_f32_16x16x128_f8f6f4 v[74:77], v[10:17], v[202:209], v[74:77], v1, v1 op_sel_hi:[0,0,0]
	v_mfma_scale_f32_16x16x128_f8f6f4 v[62:65], v[2:9], v[210:217], v[62:65], v1, v1 op_sel_hi:[0,0,0]
	v_mfma_scale_f32_16x16x128_f8f6f4 v[58:61], v[10:17], v[210:217], v[58:61], v1, v1 op_sel_hi:[0,0,0]
	v_mfma_scale_f32_16x16x128_f8f6f4 v[46:49], v[2:9], v[218:225], v[46:49], v1, v1 op_sel_hi:[0,0,0]
	v_mfma_scale_f32_16x16x128_f8f6f4 v[42:45], v[10:17], v[218:225], v[42:45], v1, v1 op_sel_hi:[0,0,0]
	s_setprio 0
	s_setprio 1
	v_mfma_scale_f32_16x16x128_f8f6f4 v[86:89], v[18:25], v[194:201], v[86:89], v1, v1 op_sel_hi:[0,0,0]
	v_mfma_scale_f32_16x16x128_f8f6f4 v[82:85], v[26:33], v[194:201], v[82:85], v1, v1 op_sel_hi:[0,0,0]
	v_mfma_scale_f32_16x16x128_f8f6f4 v[70:73], v[18:25], v[202:209], v[70:73], v1, v1 op_sel_hi:[0,0,0]
	v_mfma_scale_f32_16x16x128_f8f6f4 v[66:69], v[26:33], v[202:209], v[66:69], v1, v1 op_sel_hi:[0,0,0]
	v_mfma_scale_f32_16x16x128_f8f6f4 v[54:57], v[18:25], v[210:217], v[54:57], v1, v1 op_sel_hi:[0,0,0]
	v_mfma_scale_f32_16x16x128_f8f6f4 v[50:53], v[26:33], v[210:217], v[50:53], v1, v1 op_sel_hi:[0,0,0]
	v_mfma_scale_f32_16x16x128_f8f6f4 v[38:41], v[18:25], v[218:225], v[38:41], v1, v1 op_sel_hi:[0,0,0]
	v_mfma_scale_f32_16x16x128_f8f6f4 v[34:37], v[26:33], v[218:225], v[34:37], v1, v1 op_sel_hi:[0,0,0]
	s_setprio 0
	s_barrier
	s_add_i32 s60, s60, 2
	s_add_u32 s30, s30, 0x100
	s_addc_u32 s31, s31, 0
	s_add_u32 s58, s58, 0x100
	s_addc_u32 s59, s59, 0
	s_cmp_gt_u32 s60, 29
	s_cbranch_scc0 .LBB0_1681
	s_and_b64 vcc, exec, s[12:13]
	s_cbranch_vccz .LBB0_1684
	s_barrier
